# stack18_swap
# speedup vs baseline: 1.0230x; 1.0053x over previous
.Lsort_skip:
	s_barrier
	s_add_u32 s9, s9, 1
	s_cmp_lt_u32 s9, 16
	s_cbranch_scc1 .Lsort_turn
	ds_read_b32 v15, v14
	s_load_dwordx2 s[4:5], s[0:1], 0x20
	s_waitcnt lgkmcnt(0)
	v_mov_b32_e32 v14, v21
	v_add_u32_e32 v14, v14, v15
	v_ashrrev_i32_e32 v16, 8, v14
	v_sub_u32_e32 v17, 15, v16
	v_cmp_gt_i32_e64 s[2:3], 8, v16
	v_lshrrev_b32_e32 v15, 6, v14
	s_nop 0
	v_cndmask_b32_e64 v16, v17, v16, s[2:3]
	v_cndmask_b32_e64 v17, 4, 0, s[2:3]
	v_mov_b32_e32 v20, 0x90
	v_lshrrev_b32_e32 v20, v16, v20
	v_and_b32_e32 v20, 1, v20
	v_mul_u32_u24_e32 v20, 3, v20
	v_xor_b32_e32 v16, v16, v20
	v_and_or_b32 v17, v15, 3, v17
	v_and_b32_e32 v20, 4, v16
	v_xor_b32_e32 v17, v17, v20
	v_lshlrev_b32_e32 v15, 6, v16
	v_lshl_add_u32 v15, v17, 9, v15
	v_and_or_b32 v14, v14, 63, v15
	v_ashrrev_i32_e32 v15, 31, v14
	v_lshl_add_u64 v[14:15], v[14:15], 2, s[6:7]
	global_store_dword v[14:15], v0, off
	v_lshlrev_b32_e32 v14, 2, v17
	v_lshl_or_b32 v14, v16, 5, v14
	ds_max_i32 v14, v12 offset:768
	ds_read_b32 v12, v13
	s_waitcnt lgkmcnt(0)
	v_mov_b32_e32 v13, v22
	v_add_u32_e32 v12, v13, v12
	v_ashrrev_i32_e32 v14, 8, v12
	v_sub_u32_e32 v15, 15, v14
	v_cmp_gt_i32_e64 s[2:3], 8, v14
	v_lshrrev_b32_e32 v13, 6, v12
	s_nop 0
	v_cndmask_b32_e64 v14, v15, v14, s[2:3]
	v_cndmask_b32_e64 v15, 4, 0, s[2:3]
	v_mov_b32_e32 v20, 0x90
	v_lshrrev_b32_e32 v20, v14, v20
	v_and_b32_e32 v20, 1, v20
	v_mul_u32_u24_e32 v20, 3, v20
	v_xor_b32_e32 v14, v14, v20
	v_and_or_b32 v15, v13, 3, v15
	v_and_b32_e32 v20, 4, v14
	v_xor_b32_e32 v15, v15, v20
	v_lshlrev_b32_e32 v13, 6, v14
	v_lshl_add_u32 v13, v15, 9, v13
	v_and_or_b32 v12, v12, 63, v13
	v_ashrrev_i32_e32 v13, 31, v12
	v_lshl_add_u64 v[12:13], v[12:13], 2, s[6:7]
	global_store_dword v[12:13], v8, off
	v_lshlrev_b32_e32 v8, 2, v15
	v_lshl_or_b32 v8, v14, 5, v8
	ds_max_i32 v8, v10 offset:768
	ds_read_b32 v8, v11
	s_waitcnt lgkmcnt(0)
	v_mov_b32_e32 v10, v23
	v_add_u32_e32 v8, v10, v8
	v_ashrrev_i32_e32 v11, 8, v8
	v_sub_u32_e32 v12, 15, v11
	v_cmp_gt_i32_e64 s[2:3], 8, v11
	v_lshrrev_b32_e32 v10, 6, v8
	s_nop 0
	v_cndmask_b32_e64 v12, v12, v11, s[2:3]
	v_cndmask_b32_e64 v11, 4, 0, s[2:3]
	v_mov_b32_e32 v20, 0x90
	v_lshrrev_b32_e32 v20, v12, v20
	v_and_b32_e32 v20, 1, v20
	v_mul_u32_u24_e32 v20, 3, v20
	v_xor_b32_e32 v12, v12, v20
	v_and_or_b32 v13, v10, 3, v11
	v_and_b32_e32 v20, 4, v12
	v_xor_b32_e32 v13, v13, v20
	v_lshlrev_b32_e32 v10, 6, v12
	v_lshl_add_u32 v10, v13, 9, v10
	v_and_or_b32 v10, v8, 63, v10
	v_ashrrev_i32_e32 v11, 31, v10
	v_lshl_add_u64 v[10:11], v[10:11], 2, s[6:7]
	global_store_dword v[10:11], v6, off
	v_lshlrev_b32_e32 v6, 2, v13
	v_lshl_or_b32 v6, v12, 5, v6
	ds_max_i32 v6, v7 offset:768
	ds_read_b32 v6, v9
	s_waitcnt lgkmcnt(0)
	v_mov_b32_e32 v3, v24
	v_add_u32_e32 v3, v3, v6
	v_ashrrev_i32_e32 v7, 8, v3
	v_sub_u32_e32 v8, 15, v7
	v_cmp_gt_i32_e64 s[2:3], 8, v7
	v_lshrrev_b32_e32 v6, 6, v3
	s_nop 0
	v_cndmask_b32_e64 v8, v8, v7, s[2:3]
	v_cndmask_b32_e64 v7, 4, 0, s[2:3]
	v_mov_b32_e32 v20, 0x90
	v_lshrrev_b32_e32 v20, v8, v20
	v_and_b32_e32 v20, 1, v20
	v_mul_u32_u24_e32 v20, 3, v20
	v_xor_b32_e32 v8, v8, v20
	v_and_or_b32 v9, v6, 3, v7
	v_and_b32_e32 v20, 4, v8
	v_xor_b32_e32 v9, v9, v20
	v_lshlrev_b32_e32 v6, 6, v8
	v_lshl_add_u32 v6, v9, 9, v6
	v_and_or_b32 v6, v3, 63, v6
	v_ashrrev_i32_e32 v7, 31, v6
	v_lshl_add_u64 v[6:7], v[6:7], 2, s[6:7]
	v_lshlrev_b32_e32 v3, 2, v9
	global_store_dword v[6:7], v4, off
	v_lshl_or_b32 v3, v8, 5, v3
	ds_max_i32 v3, v5 offset:768
	s_waitcnt lgkmcnt(0)
	s_barrier
	s_and_saveexec_b64 s[6:7], vcc
	s_cbranch_execz .LBB0_14
	v_and_b32_e32 v3, 60, v0
	v_add_u32_e32 v5, 1, v0
	v_sub_u32_e32 v6, v5, v3
	v_cmp_lt_u32_e64 s[2:3], 1, v6
	s_mov_b64 s[10:11], -1
	v_mov_b32_e32 v4, 0
	s_and_saveexec_b64 s[8:9], s[2:3]
	s_cbranch_execz .LBB0_9
	v_and_b32_e32 v5, 1, v5
	v_sub_u32_e32 v4, v6, v5
	v_mov_b32_e32 v6, 0x300
	v_lshl_or_b32 v7, v3, 2, v6
	v_mov_b32_e32 v6, 0
	s_mov_b64 s[10:11], 0
	v_mov_b32_e32 v9, v4
	v_mov_b32_e32 v8, 0
